# attention main loop head aligned to 64 bytes (code placement)
# baseline (speedup 1.0000x reference)
.LBB0_334:
	s_and_b64 vcc, exec, s[60:61]
	s_cbranch_vccz .LBB0_242
	v_readlane_b32 s10, v254, 20
	s_add_u32 s10, s10, s56
	v_readlane_b32 s11, v254, 19
	s_addc_u32 s11, s11, s57
	s_add_u32 s14, s10, s58
	s_addc_u32 s15, s11, s59
	s_lshl_b64 s[90:91], s[54:55], 1
	s_add_u32 s10, s73, s90
	v_readfirstlane_b32 s11, v235
	s_addc_u32 s44, s75, s91
	s_lshr_b32 s42, s11, 6
	s_lshl_b32 s53, s42, 5
	s_mul_i32 s54, s42, 0xc000
	s_mul_hi_u32 s55, s53, 0x600
	s_lshl_b64 vcc, s[54:55], 1
	s_add_u32 s62, s10, vcc_lo
	s_addc_u32 s63, s44, vcc_hi
	s_lshl_b32 s10, s42, 4
	v_add_u32_e32 v165, s10, v208
	v_and_or_b32 v0, s10, 48, v201
	s_lshr_b32 s10, s11, 3
	s_and_b32 s10, s10, 0x1fffffe0
	s_lshl_b32 s44, s42, 10
	v_mov_b32_e32 v2, s10
	s_movk_i32 s10, 0x180
	s_cmp_lg_u32 0, -1
	v_mad_u32_u24 v0, v0, s10, v2
	s_cselect_b32 s10, 0, 0
	s_add_i32 s70, s44, s10
	v_or_b32_e32 v0, v0, v209
	s_add_i32 s10, s70, 0xc000
	s_mov_b32 m0, s70
	s_nop 0
	global_load_lds_dwordx4 v165, s[88:89]
	v_lshlrev_b32_e32 v164, 1, v0
	s_mov_b32 m0, s10
	s_nop 0
	global_load_lds_dwordx4 v164, s[14:15]
	s_add_u32 s54, s88, 0xc000
	s_addc_u32 s55, s89, 0
	s_add_i32 s71, s70, 0x2000
	s_mov_b32 m0, s71
	s_nop 0
	global_load_lds_dwordx4 v165, s[54:55]
	global_load_dwordx4 v[140:143], v217, s[62:63]
	global_load_dwordx4 v[128:131], v217, s[62:63] offset:32
	global_load_dwordx4 v[136:139], v217, s[62:63] offset:64
	global_load_dwordx4 v[132:135], v217, s[62:63] offset:96
	s_add_u32 s64, s88, 0x18000
	s_addc_u32 s65, s89, 0
	s_add_i32 s76, s70, 0x4000
	s_add_u32 s62, s88, 0x24000
	s_mov_b32 m0, s76
	s_nop 0
	global_load_lds_dwordx4 v165, s[64:65]
	s_addc_u32 s63, s89, 0
	s_add_i32 s77, s70, 0x6000
	s_mov_b32 m0, s77
	s_nop 0
	global_load_lds_dwordx4 v165, s[62:63]
	s_add_u32 s62, s14, 0xc000
	s_addc_u32 s63, s15, 0
	s_add_i32 s78, s70, 0xe000
	s_mov_b32 m0, s78
	s_nop 0
	global_load_lds_dwordx4 v164, s[62:63]
	s_add_u32 s62, s88, 0x30000
	s_addc_u32 s63, s89, 0
	s_add_i32 s79, s70, 0x8000
	s_mov_b32 m0, s79
	s_nop 0
	global_load_lds_dwordx4 v165, s[62:63]
	s_add_u32 s62, s88, 0x3c000
	s_addc_u32 s63, s89, 0
	s_add_i32 s85, s70, 0xa000
	s_mov_b32 m0, s85
	s_nop 0
	global_load_lds_dwordx4 v165, s[62:63]
	s_add_u32 s62, s14, 0x18000
	s_addc_u32 s63, s15, 0
	s_add_i32 s92, s70, 0x10000
	s_mov_b32 m0, s92
	s_nop 0
	global_load_lds_dwordx4 v164, s[62:63]
	s_add_u32 s62, s14, 0x24000
	s_addc_u32 s63, s15, 0
	s_add_i32 s93, s70, 0x12000
	s_mov_b32 m0, s93
	s_nop 0
	global_load_lds_dwordx4 v164, s[62:63]
	s_waitcnt vmcnt(7) lgkmcnt(0)
	s_barrier
	s_waitcnt vmcnt(22)
	ds_read_b128 v[36:39], v210
	s_waitcnt vmcnt(21)
	ds_read_b128 v[40:43], v210 offset:512
	s_mov_b32 s53, s52
	s_mov_b32 s54, s52
	s_mov_b32 s55, s52
	s_mov_b32 s56, s52
	s_mov_b32 s57, s52
	s_mov_b32 s58, s52
	s_mov_b32 s59, s52
	s_mov_b32 s60, s52
	s_mov_b32 s61, s52
	s_mov_b32 s62, s52
	s_mov_b32 s63, s52
	s_mov_b32 s64, s52
	s_mov_b32 s65, s52
	s_mov_b32 s66, s52
	s_mov_b32 s67, s52
	s_waitcnt vmcnt(13)
	v_mov_b64_e32 v[4:5], s[52:53]
	v_mov_b64_e32 v[6:7], s[54:55]
	v_mov_b64_e32 v[8:9], s[56:57]
	v_mov_b64_e32 v[10:11], s[58:59]
	v_mov_b64_e32 v[12:13], s[60:61]
	v_mov_b64_e32 v[14:15], s[62:63]
	v_mov_b64_e32 v[16:17], s[64:65]
	v_mov_b64_e32 v[18:19], s[66:67]
	v_mov_b32_e32 v148, 0
	v_mov_b32_e32 v2, 0
	v_mov_b32_e32 v72, 0
	s_mov_b32 s53, -5
	s_waitcnt lgkmcnt(1)
	v_mfma_f32_32x32x16_bf16 v[20:35], v[36:39], v[140:143], v[4:19]
	s_mov_b64 s[54:55], 0
	v_mov_b32_e32 v73, 0
	v_mov_b32_e32 v149, v148
	v_mov_b32_e32 v150, v148
	v_mov_b32_e32 v151, v148
	s_waitcnt lgkmcnt(0)
	v_mfma_f32_32x32x16_bf16 v[4:19], v[40:43], v[140:143], v[4:19]
	ds_read_b128 v[36:39], v210 offset:2048
	ds_read_b128 v[40:43], v210 offset:2560
	s_waitcnt lgkmcnt(1)
	v_mfma_f32_32x32x16_bf16 v[20:35], v[36:39], v[128:131], v[20:35]
	s_waitcnt lgkmcnt(0)
	v_mfma_f32_32x32x16_bf16 v[4:19], v[40:43], v[128:131], v[4:19]
	ds_read_b128 v[36:39], v210 offset:4096
	ds_read_b128 v[40:43], v210 offset:4608
	s_waitcnt lgkmcnt(1)
	v_mfma_f32_32x32x16_bf16 v[20:35], v[36:39], v[136:139], v[20:35]
	s_waitcnt lgkmcnt(0)
	v_mfma_f32_32x32x16_bf16 v[4:19], v[40:43], v[136:139], v[4:19]
	ds_read_b128 v[36:39], v210 offset:6144
	ds_read_b128 v[40:43], v210 offset:6656
	s_waitcnt lgkmcnt(1)
	v_mfma_f32_32x32x16_bf16 v[20:35], v[36:39], v[132:135], v[20:35]
	s_waitcnt lgkmcnt(0)
	v_mfma_f32_32x32x16_bf16 v[4:19], v[40:43], v[132:135], v[4:19]
	s_nop 15
	s_nop 7
	s_waitcnt vmcnt(4) lgkmcnt(0)
	s_barrier
	ds_read_b128 v[68:71], v210 offset:8192
	ds_read_b128 v[160:163], v210 offset:8704
	ds_read_b128 v[156:159], v210 offset:10240
	ds_read_b128 v[112:115], v210 offset:10752
	ds_read_b128 v[152:155], v210 offset:12288
	ds_read_b128 v[104:107], v210 offset:12800
	ds_read_b128 v[108:111], v210 offset:14336
	ds_read_b128 v[100:103], v210 offset:14848
	s_nop 1
	v_exp_f32_e32 v52, v20
	v_exp_f32_e32 v53, v21
	v_exp_f32_e32 v54, v22
	v_exp_f32_e32 v55, v23
	v_exp_f32_e32 v56, v24
	v_exp_f32_e32 v57, v25
	v_exp_f32_e32 v58, v26
	v_exp_f32_e32 v59, v27
	v_exp_f32_e32 v60, v28
	v_exp_f32_e32 v61, v29
	v_exp_f32_e32 v62, v30
	v_exp_f32_e32 v63, v31
	v_exp_f32_e32 v64, v32
	v_exp_f32_e32 v65, v33
	v_exp_f32_e32 v66, v34
	v_exp_f32_e32 v67, v35
	v_exp_f32_e32 v36, v4
	v_exp_f32_e32 v37, v5
	v_exp_f32_e32 v38, v6
	v_exp_f32_e32 v39, v7
	v_exp_f32_e32 v40, v8
	v_exp_f32_e32 v41, v9
	v_exp_f32_e32 v42, v10
	v_exp_f32_e32 v43, v11
	v_mov_b32_e32 v44, v12
	v_mov_b32_e32 v45, v13
	v_mov_b32_e32 v46, v14
	v_mov_b32_e32 v47, v15
	v_mov_b32_e32 v48, v16
	v_mov_b32_e32 v49, v17
	v_mov_b32_e32 v50, v18
	v_mov_b32_e32 v51, v19
	s_waitcnt vmcnt(4) lgkmcnt(0)
	s_barrier
	v_mov_b32_e32 v4, 0
	v_mov_b32_e32 v5, v2
	v_mov_b32_e32 v6, v2
	v_mov_b32_e32 v7, v2
	v_mov_b32_e32 v8, v2
	v_mov_b32_e32 v9, v2
	v_mov_b32_e32 v10, v2
	v_mov_b32_e32 v11, v2
	v_mov_b32_e32 v12, v2
	v_mov_b32_e32 v13, v2
	v_mov_b32_e32 v14, v2
	v_mov_b32_e32 v15, v2
	v_mov_b32_e32 v16, v2
	v_mov_b32_e32 v17, v2
	v_mov_b32_e32 v18, v2
	v_mov_b32_e32 v19, v2
	v_mov_b32_e32 v20, 0
	v_mov_b32_e32 v21, v2
	v_mov_b32_e32 v22, v2
	v_mov_b32_e32 v23, v2
	v_mov_b32_e32 v24, v2
	v_mov_b32_e32 v25, v2
	v_mov_b32_e32 v26, v2
	v_mov_b32_e32 v27, v2
	v_mov_b32_e32 v28, v2
	v_mov_b32_e32 v29, v2
	v_mov_b32_e32 v30, v2
	v_mov_b32_e32 v31, v2
	v_mov_b32_e32 v32, v2
	v_mov_b32_e32 v33, v2
	v_mov_b32_e32 v34, v2
	v_mov_b32_e32 v35, v2
	.p2align	6
